# moe_table: tile-base prefix and tile->list lookup read the 24-word LDS table with 6 ds_read_b128 and work in registers (were one word per LDS round trip, 47 in series)
# speedup vs baseline: 1.0069x; 1.0041x over previous
.LBB0_1491:
	s_or_b64 exec, exec, s[0:1]
	v_cmp_eq_u32_e64 s[0:1], 0, v128
	s_waitcnt lgkmcnt(0)
	s_barrier
	s_and_saveexec_b64 s[2:3], s[0:1]
	s_cbranch_execz .LBB0_1493
	v_readlane_b32 s5, v252, 54
	s_nop 1
	v_mov_b32_e32 v246, s5
	ds_read_b128 v[196:199], v246
	ds_read_b128 v[200:203], v246 offset:16
	ds_read_b128 v[204:207], v246 offset:32
	ds_read_b128 v[232:235], v246 offset:48
	ds_read_b128 v[236:239], v246 offset:64
	ds_read_b128 v[240:243], v246 offset:80
	v_readlane_b32 s5, v252, 53
	v_mov_b32_e32 v244, 0
	s_waitcnt lgkmcnt(0)
	v_add_u32_e32 v245, 0xff, v196
	v_ashrrev_i32_e32 v245, 8, v245
	v_mov_b32_e32 v196, v244
	v_add_u32_e32 v244, v244, v245
	v_add_u32_e32 v245, 0xff, v197
	v_ashrrev_i32_e32 v245, 8, v245
	v_mov_b32_e32 v197, v244
	v_add_u32_e32 v244, v244, v245
	v_add_u32_e32 v245, 0xff, v198
	v_ashrrev_i32_e32 v245, 8, v245
	v_mov_b32_e32 v198, v244
	v_add_u32_e32 v244, v244, v245
	v_add_u32_e32 v245, 0xff, v199
	v_ashrrev_i32_e32 v245, 8, v245
	v_mov_b32_e32 v199, v244
	v_add_u32_e32 v244, v244, v245
	v_add_u32_e32 v245, 0xff, v200
	v_ashrrev_i32_e32 v245, 8, v245
	v_mov_b32_e32 v200, v244
	v_add_u32_e32 v244, v244, v245
	v_add_u32_e32 v245, 0xff, v201
	v_ashrrev_i32_e32 v245, 8, v245
	v_mov_b32_e32 v201, v244
	v_add_u32_e32 v244, v244, v245
	v_add_u32_e32 v245, 0xff, v202
	v_ashrrev_i32_e32 v245, 8, v245
	v_mov_b32_e32 v202, v244
	v_add_u32_e32 v244, v244, v245
	v_add_u32_e32 v245, 0xff, v203
	v_ashrrev_i32_e32 v245, 8, v245
	v_mov_b32_e32 v203, v244
	v_add_u32_e32 v244, v244, v245
	v_add_u32_e32 v245, 0xff, v204
	v_ashrrev_i32_e32 v245, 8, v245
	v_mov_b32_e32 v204, v244
	v_add_u32_e32 v244, v244, v245
	v_add_u32_e32 v245, 0xff, v205
	v_ashrrev_i32_e32 v245, 8, v245
	v_mov_b32_e32 v205, v244
	v_add_u32_e32 v244, v244, v245
	v_add_u32_e32 v245, 0xff, v206
	v_ashrrev_i32_e32 v245, 8, v245
	v_mov_b32_e32 v206, v244
	v_add_u32_e32 v244, v244, v245
	v_add_u32_e32 v245, 0xff, v207
	v_ashrrev_i32_e32 v245, 8, v245
	v_mov_b32_e32 v207, v244
	v_add_u32_e32 v244, v244, v245
	v_add_u32_e32 v245, 0xff, v232
	v_ashrrev_i32_e32 v245, 8, v245
	v_mov_b32_e32 v232, v244
	v_add_u32_e32 v244, v244, v245
	v_add_u32_e32 v245, 0xff, v233
	v_ashrrev_i32_e32 v245, 8, v245
	v_mov_b32_e32 v233, v244
	v_add_u32_e32 v244, v244, v245
	v_add_u32_e32 v245, 0xff, v234
	v_ashrrev_i32_e32 v245, 8, v245
	v_mov_b32_e32 v234, v244
	v_add_u32_e32 v244, v244, v245
	v_add_u32_e32 v245, 0xff, v235
	v_ashrrev_i32_e32 v245, 8, v245
	v_mov_b32_e32 v235, v244
	v_add_u32_e32 v244, v244, v245
	v_add_u32_e32 v245, 0xff, v236
	v_ashrrev_i32_e32 v245, 8, v245
	v_mov_b32_e32 v236, v244
	v_add_u32_e32 v244, v244, v245
	v_add_u32_e32 v245, 0xff, v237
	v_ashrrev_i32_e32 v245, 8, v245
	v_mov_b32_e32 v237, v244
	v_add_u32_e32 v244, v244, v245
	v_add_u32_e32 v245, 0xff, v238
	v_ashrrev_i32_e32 v245, 8, v245
	v_mov_b32_e32 v238, v244
	v_add_u32_e32 v244, v244, v245
	v_add_u32_e32 v245, 0xff, v239
	v_ashrrev_i32_e32 v245, 8, v245
	v_mov_b32_e32 v239, v244
	v_add_u32_e32 v244, v244, v245
	v_add_u32_e32 v245, 0xff, v240
	v_ashrrev_i32_e32 v245, 8, v245
	v_mov_b32_e32 v240, v244
	v_add_u32_e32 v244, v244, v245
	v_add_u32_e32 v245, 0xff, v241
	v_ashrrev_i32_e32 v245, 8, v245
	v_mov_b32_e32 v241, v244
	v_add_u32_e32 v244, v244, v245
	v_add_u32_e32 v245, 0xff, v242
	v_ashrrev_i32_e32 v245, 8, v245
	v_mov_b32_e32 v242, v244
	v_add_u32_e32 v244, v244, v245
	v_add_u32_e32 v245, 0xff, v243
	v_ashrrev_i32_e32 v245, 8, v245
	v_mov_b32_e32 v243, v244
	v_add_u32_e32 v244, v244, v245
	v_mov_b32_e32 v246, s5
	ds_write_b128 v246, v[196:199]
	ds_write_b128 v246, v[200:203] offset:16
	ds_write_b128 v246, v[204:207] offset:32
	ds_write_b128 v246, v[232:235] offset:48
	ds_write_b128 v246, v[236:239] offset:64
	ds_write_b128 v246, v[240:243] offset:80
	ds_write_b32 v246, v244 offset:96
.LBB0_1493:
	s_or_b64 exec, exec, s[2:3]
	s_movk_i32 s2, 0xa0
	v_cmp_gt_i32_e32 vcc, s2, v128
	s_waitcnt lgkmcnt(0)
	s_barrier
	s_and_saveexec_b64 s[2:3], vcc
	s_cbranch_execz .LBB0_1495
	v_readlane_b32 s5, v252, 53
	s_nop 1
	v_mov_b32_e32 v246, s5
	ds_read_b128 v[196:199], v246
	ds_read_b128 v[200:203], v246 offset:16
	ds_read_b128 v[204:207], v246 offset:32
	ds_read_b128 v[232:235], v246 offset:48
	ds_read_b128 v[236:239], v246 offset:64
	ds_read_b128 v[240:243], v246 offset:80
	s_waitcnt lgkmcnt(0)
	v_cmp_ge_i32_e32 vcc, v128, v197
	s_nop 1
	v_cndmask_b32_e64 v1, 0, 1, vcc
	v_cmp_lt_i32_e32 vcc, v128, v198
	s_nop 1
	v_cndmask_b32_e32 v1, 2, v1, vcc
	v_cmp_lt_i32_e32 vcc, v128, v199
	s_nop 1
	v_cndmask_b32_e32 v1, 3, v1, vcc
	v_cmp_lt_i32_e32 vcc, v128, v200
	s_nop 1
	v_cndmask_b32_e32 v1, 4, v1, vcc
	v_cmp_lt_i32_e32 vcc, v128, v201
	s_nop 1
	v_cndmask_b32_e32 v1, 5, v1, vcc
	v_cmp_lt_i32_e32 vcc, v128, v202
	s_nop 1
	v_cndmask_b32_e32 v1, 6, v1, vcc
	v_cmp_lt_i32_e32 vcc, v128, v203
	s_nop 1
	v_cndmask_b32_e32 v1, 7, v1, vcc
	v_cmp_lt_i32_e32 vcc, v128, v204
	s_nop 1
	v_cndmask_b32_e32 v1, 8, v1, vcc
	v_cmp_lt_i32_e32 vcc, v128, v205
	s_nop 1
	v_cndmask_b32_e32 v1, 9, v1, vcc
	v_cmp_lt_i32_e32 vcc, v128, v206
	s_nop 1
	v_cndmask_b32_e32 v1, 10, v1, vcc
	v_cmp_lt_i32_e32 vcc, v128, v207
	s_nop 1
	v_cndmask_b32_e32 v1, 11, v1, vcc
	v_cmp_lt_i32_e32 vcc, v128, v232
	s_nop 1
	v_cndmask_b32_e32 v1, 12, v1, vcc
	v_cmp_lt_i32_e32 vcc, v128, v233
	s_nop 1
	v_cndmask_b32_e32 v1, 13, v1, vcc
	v_cmp_lt_i32_e32 vcc, v128, v234
	s_nop 1
	v_cndmask_b32_e32 v1, 14, v1, vcc
	v_cmp_lt_i32_e32 vcc, v128, v235
	s_nop 1
	v_cndmask_b32_e32 v1, 15, v1, vcc
	v_cmp_lt_i32_e32 vcc, v128, v236
	s_nop 1
	v_cndmask_b32_e32 v1, 16, v1, vcc
	v_cmp_lt_i32_e32 vcc, v128, v237
	s_nop 1
	v_cndmask_b32_e32 v1, 17, v1, vcc
	v_cmp_lt_i32_e32 vcc, v128, v238
	s_nop 1
	v_cndmask_b32_e32 v1, 18, v1, vcc
	v_cmp_lt_i32_e32 vcc, v128, v239
	s_nop 1
	v_cndmask_b32_e32 v1, 19, v1, vcc
	v_cmp_lt_i32_e32 vcc, v128, v240
	s_nop 1
	v_cndmask_b32_e32 v1, 20, v1, vcc
	v_cmp_lt_i32_e32 vcc, v128, v241
	s_nop 1
	v_cndmask_b32_e32 v1, 21, v1, vcc
	v_cmp_lt_i32_e32 vcc, v128, v242
	s_nop 1
	v_cndmask_b32_e32 v1, 22, v1, vcc
	v_cmp_lt_i32_e32 vcc, v128, v243
	s_nop 1
	v_cndmask_b32_e32 v1, 23, v1, vcc
	ds_write_b32 v0, v1 offset:256
